# v10: v8 + static s_setprio 1 for the scan state waves (critical path), helpers at 0
# speedup vs baseline: 1.0249x; 1.0249x over previous
.LBB0_1721:
	s_and_b32 s56, s83, 31
	s_bfe_u32 s73, s83, 0x10005
	s_lshl_b32 s72, s56, 6
	s_cmp_lt_u32 s83, 64
	s_cselect_b64 s[28:29], -1, 0
	s_and_b64 s[66:67], s[28:29], exec
	s_mov_b32 s0, 0x8c00000
	s_cselect_b32 s0, s0, 0x29400000
	s_add_u32 s66, s54, s0
	s_addc_u32 s67, s55, 0
	s_andn2_b64 vcc, exec, s[50:51]
	s_mov_b64 s[68:69], -1
	s_cbranch_vccnz .LBB0_1737
	s_setprio 1
	s_and_saveexec_b64 s[68:69], s[4:5]
	v_mov_b32_e32 v2, s61
	ds_write_b32 v2, v161
	s_or_b64 exec, exec, s[68:69]
	s_lshl_b32 s0, s72, 1
	s_add_u32 s0, s66, s0
	s_addc_u32 s1, s67, 0
	s_add_u32 s0, s0, s81
	s_addc_u32 s1, s1, 0
	v_lshlrev_b32_e32 v160, 1, v158
	v_mov_b32_e32 v2, 0
	v_lshl_add_u64 v[164:165], s[0:1], 0, v[160:161]
	s_lshl_b32 s70, s73, 14
	s_mov_b32 s71, 0
	v_mov_b32_e32 v3, v2
	v_mov_b32_e32 v4, v2
	v_mov_b32_e32 v5, v2
	v_mov_b32_e32 v10, v2
	v_mov_b32_e32 v11, v2
	v_mov_b32_e32 v12, v2
	v_mov_b32_e32 v13, v2
	v_mov_b32_e32 v6, v2
	v_mov_b32_e32 v7, v2
	v_mov_b32_e32 v8, v2
	v_mov_b32_e32 v9, v2
	v_mov_b32_e32 v14, v2
	v_mov_b32_e32 v15, v2
	v_mov_b32_e32 v16, v2
	v_mov_b32_e32 v17, v2
	v_and_b32_e32 v25, 1, v0
	v_cmp_ne_u32_e64 s[98:99], 0, v25
	v_add_u32_e32 v24, v184, v25
	v_add_u32_e32 v22, 0xffffff00, v24
	v_sub_u32_e32 v23, 0x40ff, v24
	v_cndmask_b32_e64 v22, v23, v22, s[28:29]
	v_add_u32_e32 v22, s70, v22
	v_ashrrev_i32_e32 v23, 31, v22
	v_lshlrev_b64 v[22:23], 12, v[22:23]
	v_lshl_add_u64 v[22:23], v[164:165], 0, v[22:23]
	v_sub_u32_e32 v27, 0, v25
	v_lshlrev_b32_e32 v26, 1, v27
	v_lshl_add_u64 v[210:211], v[22:23], 0, v[26:27]
	v_mov_b32_e32 v28, 0x2000
	v_mov_b32_e32 v29, 0xffffe000
	v_cndmask_b32_e64 v28, v29, v28, s[28:29]
	v_ashrrev_i32_e32 v29, 31, v28
	v_lshl_add_u64 v[212:213], v[210:211], 0, v[28:29]
	s_mov_b32 s100, 0x10000
	s_mov_b32 s101, 0
	s_cmp_lt_u32 s83, 64
	s_cbranch_scc1 .Lx14_dir0
	s_mov_b32 s100, 0xffff0000
	s_mov_b32 s101, -1

.LBB0_1736:
	s_setprio 0
	s_mov_b64 s[68:69], 0
